# scan: prefetch next step's u0/u1/gl one step ahead, counted vmcnt(16) instead of vmcnt(0) at step top
# baseline (speedup 1.0000x reference)
.LBB0_606:
	s_and_b32 s6, s34, 0x3ffffffc
	s_add_i32 s28, s6, s2
	s_and_b64 s[6:7], s[38:39], exec
	s_cselect_b32 s6, s34, s28
	s_mul_i32 s36, s6, 0x44
	s_mul_i32 s6, s6, 0x2a8000
	s_mul_hi_i32 s7, s36, 0xa000
	s_add_u32 s28, s10, s6
	s_addc_u32 s29, s11, s7
	s_add_u32 s6, s28, s12
	s_addc_u32 s7, s29, 0
	s_mov_b32 m0, s13
	v_lshl_add_u64 v[0:1], s[6:7], 0, v[44:45]
	s_waitcnt vmcnt(0)
	s_barrier
	global_load_lds_dwordx4 v[0:1], off
	v_lshl_add_u64 v[2:3], v[0:1], 0, s[72:73]
	s_add_i32 m0, s13, 0x400
	v_mov_b32_e32 v64, v62
	global_load_lds_dwordx4 v[2:3], off
	v_lshl_add_u64 v[2:3], v[0:1], 0, s[80:81]
	s_add_i32 m0, s13, 0x800
	v_lshl_add_u64 v[0:1], v[0:1], 0, s[64:65]
	global_load_lds_dwordx4 v[2:3], off
	s_add_i32 m0, s13, 0xc00
	s_add_u32 s6, s28, s14
	global_load_lds_dwordx4 v[0:1], off
	s_addc_u32 s7, s29, 0
	s_add_i32 m0, s13, 0x1000
	v_lshl_add_u64 v[0:1], s[6:7], 0, v[44:45]
	s_add_u32 s6, s28, s25
	global_load_lds_dwordx4 v[0:1], off
	s_addc_u32 s7, s29, 0
	s_add_i32 m0, s13, 0x1400
	v_lshl_add_u64 v[0:1], s[6:7], 0, v[44:45]
	s_add_u32 s6, s28, s27
	global_load_lds_dwordx4 v[0:1], off
	s_addc_u32 s7, s29, 0
	s_add_i32 m0, s13, 0x1800
	v_lshl_add_u64 v[0:1], s[6:7], 0, v[44:45]
	s_add_u32 s6, s28, s33
	s_addc_u32 s7, s29, 0
	global_load_lds_dwordx4 v[0:1], off
	v_lshl_add_u64 v[0:1], s[6:7], 0, v[44:45]
	s_add_i32 m0, s13, 0x1c00
	s_ashr_i32 s37, s34, 2
	global_load_lds_dwordx4 v[0:1], off
	v_mov_b32_e32 v0, 0
	s_mul_hi_i32 s7, s37, 0x1100
	s_mul_i32 s6, s37, 0x1100
	s_mov_b32 s28, 0
	s_mov_b32 s48, 0
	s_mov_b32 s49, 0
	v_mov_b32_e32 v1, v0
	v_mov_b32_e32 v2, v0
	v_mov_b32_e32 v3, v0
	v_mov_b32_e32 v4, v0
	v_mov_b32_e32 v5, v0
	v_mov_b32_e32 v6, v0
	v_mov_b32_e32 v7, v0
	v_mov_b32_e32 v8, v0
	v_mov_b32_e32 v9, v0
	v_mov_b32_e32 v10, v0
	v_mov_b32_e32 v11, v0
	v_mov_b32_e32 v12, v0
	v_mov_b32_e32 v13, v0
	v_mov_b32_e32 v14, v0
	v_mov_b32_e32 v15, v0
	s_mul_i32 s30, s36, 0xa000
	s_mul_hi_i32 s31, s36, 0xa000
	s_add_u32 s30, s18, s30
	s_addc_u32 s31, s19, s31
	v_lshl_add_u64 v[16:17], s[30:31], 0, v[46:47]
	s_mov_b64 s[30:31], 0x44008000
	s_mov_b32 s98, s36
	s_ashr_i32 s99, s36, 31
	v_lshl_add_u64 v[16:17], v[16:17], 0, s[30:31]
	s_lshl_b64 s[98:99], s[98:99], 2
	s_add_u32 s98, s67, s98
	s_addc_u32 s99, s0, s99
	global_load_dwordx4 v[180:183], v[16:17], off
	global_load_dwordx4 v[184:187], v[16:17], off offset:16
	global_load_dword v188, v113, s[98:99]
	s_waitcnt vmcnt(0)
	s_branch .LBB0_608

.LBB0_608:
	s_add_i32 s42, s36, s49
	s_waitcnt vmcnt(16)
	v_mov_b32_e32 v28, v180
	v_mov_b32_e32 v29, v181
	v_mov_b32_e32 v30, v182
	v_mov_b32_e32 v31, v183
	v_mov_b32_e32 v24, v184
	v_mov_b32_e32 v25, v185
	v_mov_b32_e32 v26, v186
	v_mov_b32_e32 v27, v187
	v_mov_b32_e32 v58, v188
	s_cmpk_lg_i32 s48, 0x10c0
	s_mov_b64 s[46:47], -1
	s_waitcnt lgkmcnt(0)
	s_barrier
	s_cbranch_scc0 .LBB0_610
	s_add_i32 s43, s28, 0x10000
	s_add_i32 s30, s42, 1
	s_and_b32 s29, s43, 0x10000
	s_mul_hi_i32 s31, s30, 0xa000
	s_mul_i32 s30, s30, 0xa000
	s_add_u32 s30, s10, s30
	s_addc_u32 s31, s11, s31
	s_add_u32 s46, s30, s12
	s_addc_u32 s47, s31, 0
	s_add_i32 s29, s13, s29
	v_lshl_add_u64 v[16:17], s[46:47], 0, v[44:45]
	s_mov_b32 m0, s29
	v_lshl_add_u64 v[18:19], v[16:17], 0, s[72:73]
	global_load_lds_dwordx4 v[16:17], off
	s_add_i32 m0, s29, 0x400
	s_nop 0
	global_load_lds_dwordx4 v[18:19], off
	v_lshl_add_u64 v[18:19], v[16:17], 0, s[80:81]
	s_add_i32 m0, s29, 0x800
	v_lshl_add_u64 v[16:17], v[16:17], 0, s[64:65]
	global_load_lds_dwordx4 v[18:19], off
	s_add_i32 m0, s29, 0xc00
	s_add_u32 s46, s30, s14
	global_load_lds_dwordx4 v[16:17], off
	s_addc_u32 s47, s31, 0
	s_add_i32 m0, s29, 0x1000
	v_lshl_add_u64 v[16:17], s[46:47], 0, v[44:45]
	s_add_u32 s46, s30, s25
	global_load_lds_dwordx4 v[16:17], off
	s_addc_u32 s47, s31, 0
	s_add_i32 m0, s29, 0x1400
	v_lshl_add_u64 v[16:17], s[46:47], 0, v[44:45]
	s_add_u32 s46, s30, s27
	global_load_lds_dwordx4 v[16:17], off
	s_addc_u32 s47, s31, 0
	s_add_i32 m0, s29, 0x1800
	v_lshl_add_u64 v[16:17], s[46:47], 0, v[44:45]
	s_add_u32 s46, s30, s33
	s_addc_u32 s47, s31, 0
	global_load_lds_dwordx4 v[16:17], off
	v_lshl_add_u64 v[16:17], s[46:47], 0, v[44:45]
	s_add_i32 m0, s29, 0x1c00
	s_mov_b64 s[46:47], 0
	global_load_lds_dwordx4 v[16:17], off
	s_add_i32 s98, s42, 1
	s_mul_i32 s30, s98, 0xa000
	s_mul_hi_i32 s31, s98, 0xa000
	s_add_u32 s30, s18, s30
	s_addc_u32 s31, s19, s31
	v_lshl_add_u64 v[16:17], s[30:31], 0, v[46:47]
	s_mov_b64 s[30:31], 0x44008000
	s_ashr_i32 s99, s98, 31
	v_lshl_add_u64 v[16:17], v[16:17], 0, s[30:31]
	s_lshl_b64 s[98:99], s[98:99], 2
	s_add_u32 s98, s67, s98
	s_addc_u32 s99, s0, s99
	global_load_dwordx4 v[180:183], v[16:17], off
	global_load_dwordx4 v[184:187], v[16:17], off offset:16
	global_load_dword v188, v113, s[98:99]
